# block-major far-block path: tokens ordered by class so most items touch one block (one-block item), next pair's staging loads issued before the step barrier
# speedup vs baseline: 1.0081x; 1.0032x over previous
; #define LAS __attribute__((address_space(3)))
; __device__ __forceinline__ unsigned or_x16(unsigned u) { return u | __shfl_xor(u, 16); }
; __device__ __forceinline__ unsigned or_x32(unsigned u) { return u | __shfl_xor(u, 32); }
; __device__ __forceinline__ void select_blocks8(const LAS float* impw, LAS unsigned* mk, int lane, int cur, unsigned (&u)[2][4]) {
;     ...
; #pragma unroll
;     for (int c = 0; c < 2; ++c) {
;         if (i == 0) *(LAS u32x4*)(mk + (4 * c + k) * 4) = (u32x4){m4[c][0], m4[c][1], m4[c][2], m4[c][3]};
; #pragma unroll
;         for (int x = 0; x < 4; ++x) { unsigned v = m4[c][x]; v = or_x16(v); v = or_x32(v); u[c][x] = __builtin_amdgcn_readfirstlane(v); }
;     }
; __device__ __forceinline__ void nsa_unit(unsigned char* ws, LAS unsigned char* lds, const LAS float* lut, int b, int g, int tau, int tid_in) {
;     ...
; #pragma unroll
;     for (int c = 0; c < 2; ++c) { const float gc = NSA_GATE(c, 0);
; #pragma unroll
;         for (int dt = 0; dt < 4; ++dt) resw[(c * 4 + dt) * 64] = Oc[c][dt] * gc; }
.LBB0_1173:
	s_lshl_b32 s1, s91, 7
	s_add_i32 s24, s1, 0
	s_add_i32 s24, s24, 0x22d00
	v_cmp_eq_u32_e32 vcc, 0, v187
	v_add_u32_e32 v4, s24, v1
	s_and_saveexec_b64 s[6:7], vcc
	ds_write_b128 v4, v[74:77]
	s_or_b64 exec, exec, s[6:7]
	v_and_b32_e32 v5, 64, v176
	v_xor_b32_e32 v3, 16, v176
	v_add_u32_e32 v5, 64, v5
	v_cmp_lt_i32_e64 s[6:7], v3, v5
	v_xor_b32_e32 v78, 32, v176
	s_nop 0
	v_cndmask_b32_e64 v3, v176, v3, s[6:7]
	v_cmp_lt_i32_e64 s[6:7], v78, v5
	v_lshlrev_b32_e32 v3, 2, v3
	s_nop 0
	v_cndmask_b32_e64 v5, v176, v78, s[6:7]
	v_lshlrev_b32_e32 v155, 2, v5
	ds_bpermute_b32 v5, v3, v74
	s_waitcnt lgkmcnt(0)
	v_or_b32_e32 v5, v5, v74
	ds_bpermute_b32 v74, v155, v5
	s_waitcnt lgkmcnt(0)
	v_or_b32_e32 v5, v74, v5
	s_nop 0
	v_readfirstlane_b32 s17, v5
	ds_bpermute_b32 v5, v3, v75
	s_waitcnt lgkmcnt(0)
	v_or_b32_e32 v5, v5, v75
	ds_bpermute_b32 v74, v155, v5
	s_waitcnt lgkmcnt(0)
	v_or_b32_e32 v5, v74, v5
	s_nop 0
	v_readfirstlane_b32 s38, v5
	ds_bpermute_b32 v5, v3, v76
	s_waitcnt lgkmcnt(0)
	v_or_b32_e32 v5, v5, v76
	ds_bpermute_b32 v74, v155, v5
	s_waitcnt lgkmcnt(0)
	v_or_b32_e32 v5, v74, v5
	s_nop 0
	v_readfirstlane_b32 s39, v5
	ds_bpermute_b32 v5, v3, v77
	s_waitcnt lgkmcnt(0)
	v_or_b32_e32 v5, v5, v77
	ds_bpermute_b32 v74, v155, v5
	s_waitcnt lgkmcnt(0)
	v_or_b32_e32 v5, v74, v5
	s_nop 0
	v_readfirstlane_b32 s5, v5
	s_and_saveexec_b64 s[6:7], vcc
	ds_write_b128 v4, v[70:73] offset:64
	s_or_b64 exec, exec, s[6:7]
	ds_bpermute_b32 v4, v3, v70
	s_lshl_b32 s6, s2, 13
	s_mov_b32 s7, s27
	v_lshl_add_u64 v[158:159], s[6:7], 0, v[164:165]
	s_waitcnt lgkmcnt(0)
	v_or_b32_e32 v4, v4, v70
	ds_bpermute_b32 v5, v155, v4
	s_barrier
	s_waitcnt lgkmcnt(0)
	s_lshl_b32 s1, s91, 13
	s_add_i32 s1, s1, 0
	v_or_b32_e32 v74, v5, v4
	ds_bpermute_b32 v4, v3, v71
	v_lshl_add_u32 v1, v1, 4, s1
	v_add_u32_e32 v1, 0x10000, v1
	s_movk_i32 s1, 0x70
	s_andn2_b64 vcc, exec, s[50:51]
	s_waitcnt lgkmcnt(0)
	v_or_b32_e32 v4, v4, v71
	ds_bpermute_b32 v5, v155, v4
	s_waitcnt lgkmcnt(0)
	v_or_b32_e32 v75, v5, v4
	ds_bpermute_b32 v4, v3, v72
	v_readfirstlane_b32 s73, v75
	s_waitcnt lgkmcnt(0)
	v_or_b32_e32 v4, v4, v72
	ds_bpermute_b32 v5, v155, v4
	s_waitcnt lgkmcnt(0)
	v_or_b32_e32 v72, v5, v4
	ds_bpermute_b32 v4, v3, v73
	s_waitcnt lgkmcnt(0)
	v_or_b32_e32 v4, v4, v73
	ds_bpermute_b32 v5, v155, v4
	s_waitcnt lgkmcnt(0)
	v_or_b32_e32 v73, v5, v4
	v_mul_u32_u24_e32 v4, 3, v191
	v_lshlrev_b32_e32 v152, 2, v4
	v_lshl_add_u64 v[70:71], s[28:29], 0, v[152:153]
	v_mad_u64_u32 v[4:5], s[2:3], v158, s0, v[70:71]
	v_mad_i32_i24 v5, v159, s0, v5
	global_load_dword v4, v[4:5], off
	v_readfirstlane_b32 s72, v73
	s_waitcnt vmcnt(0)
	v_pk_mul_f32 v[212:213], v[56:57], v[4:5] op_sel_hi:[1,0]
	v_pk_mul_f32 v[210:211], v[54:55], v[4:5] op_sel_hi:[1,0]
	v_pk_mul_f32 v[216:217], v[60:61], v[4:5] op_sel_hi:[1,0]
	v_pk_mul_f32 v[214:215], v[58:59], v[4:5] op_sel_hi:[1,0]
	v_pk_mul_f32 v[220:221], v[64:65], v[4:5] op_sel_hi:[1,0]
	v_pk_mul_f32 v[218:219], v[62:63], v[4:5] op_sel_hi:[1,0]
	v_pk_mul_f32 v[224:225], v[68:69], v[4:5] op_sel_hi:[1,0]
	v_pk_mul_f32 v[222:223], v[66:67], v[4:5] op_sel_hi:[1,0]
	v_lshl_add_u64 v[4:5], s[6:7], 0, v[108:109]
	v_mad_u64_u32 v[54:55], s[2:3], v4, s0, v[70:71]
	v_mad_i32_i24 v55, v5, s0, v55
	global_load_dword v54, v[54:55], off
	v_readfirstlane_b32 s2, v74
	v_readfirstlane_b32 s3, v72
	s_waitcnt vmcnt(0)
	v_pk_mul_f32 v[228:229], v[40:41], v[54:55] op_sel_hi:[1,0]
	v_pk_mul_f32 v[226:227], v[38:39], v[54:55] op_sel_hi:[1,0]
	v_pk_mul_f32 v[232:233], v[44:45], v[54:55] op_sel_hi:[1,0]
	v_pk_mul_f32 v[230:231], v[42:43], v[54:55] op_sel_hi:[1,0]
	v_pk_mul_f32 v[236:237], v[48:49], v[54:55] op_sel_hi:[1,0]
	v_pk_mul_f32 v[234:235], v[46:47], v[54:55] op_sel_hi:[1,0]
	v_pk_mul_f32 v[240:241], v[52:53], v[54:55] op_sel_hi:[1,0]
	v_pk_mul_f32 v[238:239], v[50:51], v[54:55] op_sel_hi:[1,0]
	s_mov_b32 s98, 0
	s_mov_b32 s100, -1
	s_mov_b32 s101, 0
	v_and_b32_e32 v248, 3, v185
	v_lshlrev_b32_e32 v249, 2, v248
	v_lshl_add_u32 v248, v186, 6, v249
	v_add_u32_e32 v248, 0x10000, v248
	v_add_u32_e32 v249, 0x20400, v249
	v_lshlrev_b32_e32 v250, 2, v184
	v_and_b32_e32 v251, 63, v185
	v_lshlrev_b32_e32 v251, 4, v251
	v_add_u32_e32 v251, 0x22d00, v251
	ds_read_b128 v[242:245], v251
	s_waitcnt lgkmcnt(0)
	v_xor_b32_e32 v39, v110, v185
	v_lshlrev_b32_e32 v38, 7, v110
	v_lshlrev_b32_e32 v39, 4, v39
	v_and_or_b32 v38, v39, s1, v38
	v_add_u32_e32 v188, 0, v38
	v_cndmask_b32_e64 v38, 0, 1, s[50:51]
	v_cmp_ne_u32_e64 s[6:7], 1, v38
	ds_write_b128 v188, v[26:29]
	ds_write_b128 v188, v[22:25] offset:32768
	s_cbranch_vccnz .LBB0_1179
	ds_write_b128 v188, v[30:33] offset:8192
	ds_write_b128 v188, v[34:37] offset:40960

.LBB0_1182:
	s_lshr_b32 s11, s75, 3
	v_add_u32_e32 v78, s11, v165
	ds_read2_b32 v[174:175], v78 offset1:16
.LBB0_1183:
	s_add_i32 s76, s75, 2
	s_cmp_gt_i32 s76, s37
	s_cselect_b64 s[66:67], -1, 0
	s_cmp_le_i32 s76, s37
	s_cselect_b64 s[68:69], -1, 0
	s_and_b64 s[12:13], s[66:67], exec
	s_cselect_b32 s13, s79, s65
	s_cselect_b32 s12, s54, s64
	s_cselect_b32 s15, s36, s63
	s_cselect_b32 s14, s51, s62
	s_cmp_eq_u32 s101, 0
	s_cbranch_scc1 .Lbm_top_loads
	s_mov_b32 s101, 0
	s_add_i32 s11, s75, 3
	s_cmp_le_i32 s11, s37
	s_cselect_b64 s[70:71], -1, 0
	s_branch .LBB0_1185
.Lbm_top_loads:
	s_waitcnt vmcnt(3)
	v_lshl_add_u64 v[22:23], s[14:15], 0, v[162:163]
	s_waitcnt vmcnt(2)
	v_lshl_add_u64 v[26:27], s[12:13], 0, v[156:157]
	v_lshl_add_u64 v[22:23], v[22:23], 0, v[160:161]
	v_lshl_add_u64 v[26:27], v[26:27], 0, v[160:161]
	global_load_dwordx4 v[22:25], v[22:23], off
	s_add_i32 s11, s75, 3
	global_load_dwordx4 v[26:29], v[26:27], off
	s_cmp_le_i32 s11, s37
	s_cselect_b64 s[70:71], -1, 0
	s_cmp_gt_i32 s11, s37
	s_cbranch_scc1 .LBB0_1185
	v_lshl_add_u64 v[30:31], s[64:65], 0, v[166:167]
	v_add_co_u32_e32 v30, vcc, 0x8000, v30
	v_lshl_add_u64 v[34:35], s[62:63], 0, v[168:169]
	s_nop 0
	v_addc_co_u32_e32 v31, vcc, 0, v31, vcc
	global_load_dwordx4 v[30:33], v[30:31], off
	s_nop 0
	global_load_dwordx4 v[34:37], v[34:35], off offset:128

; #define LAS __attribute__((address_space(3)))
; __device__ __forceinline__ float ex2(float x) { return __builtin_amdgcn_exp2f(x); }
; template <int C>
; __device__ __forceinline__ void attn_far1_fast(const LAS unsigned char* kb, const LAS unsigned char* vb, const bf16x8 (&qf)[2][2], int col, int q, float bias_far, bool sel, Softmax (&st)[2], f32x4 (&O)[2][4]) {
;     const f32x4 z4 = (f32x4){0.f, 0.f, 0.f, 0.f};
;     const float NEG = -__builtin_inff();
;     f32x4 S[4];
; #pragma unroll
;     for (int kt = 0; kt < 4; ++kt) { const bf16x8 k0 = lds_frag(kb, 16 * kt + col, q), k1 = lds_frag(kb, 16 * kt + col, 4 + q);
;         S[kt] = __builtin_amdgcn_mfma_f32_16x16x32_bf16(k0, qf[C][0], z4, 0, 0, 0); S[kt] = __builtin_amdgcn_mfma_f32_16x16x32_bf16(k1, qf[C][1], S[kt], 0, 0, 0); }
;     const float off = (sel ? bias_far : NEG) - st[C].m;
; #pragma unroll
;     for (int kt = 0; kt < 4; ++kt) { f32x4 p = S[kt] + off;
; #pragma unroll
;         for (int e = 0; e < 4; ++e) p[e] = ex2(p[e]);
;         S[kt] = p; }
;     const bf16x8 pf0 = pack8(S[0], S[1]), pf1 = pack8(S[2], S[3]);
.Lbm_step:
	s_lshr_b32 s21, s75, 5
	v_mov_b32_e32 v79, v242
	s_cmp_eq_u32 s21, 1
	s_cselect_b64 vcc, -1, 0
	v_cndmask_b32_e32 v79, v79, v243, vcc
	s_cmp_eq_u32 s21, 2
	s_cselect_b64 vcc, -1, 0
	v_cndmask_b32_e32 v79, v79, v244, vcc
	s_cmp_eq_u32 s21, 3
	s_cselect_b64 vcc, -1, 0
	v_cndmask_b32_e32 v79, v79, v245, vcc
	s_and_b32 s21, s75, 31
	s_lshl_b32 s21, 1, s21
	s_lshl_b32 s32, s21, 1
	v_and_b32_e32 v80, s21, v79
	v_cmp_ne_u32_e64 s[12:13], 0, v80
	v_and_b32_e32 v80, s32, v79
	v_cmp_ne_u32_e64 s[14:15], 0, v80
	s_nop 3
	s_or_b64 s[22:23], s[12:13], s[14:15]
	s_bcnt1_i32_b64 s11, s[22:23]
	s_add_i32 s11, s11, 3
	s_lshr_b32 s11, s11, 2
	s_mov_b32 s21, s91
	s_mov_b32 s98, 1
	s_cmp_ge_u32 s21, s11
	s_cbranch_scc1 .Lbm_noitem
	s_andn2_b64 s[84:85], s[12:13], s[14:15]
	s_bcnt1_i32_b64 s77, s[84:85]
	v_mbcnt_lo_u32_b32 v80, s84, 0
	v_mbcnt_hi_u32_b32 v80, s85, v80
	v_mov_b32_e32 v56, s77
	s_and_b64 s[84:85], s[12:13], s[14:15]
	s_bcnt1_i32_b64 s32, s[84:85]
	v_mbcnt_lo_u32_b32 v56, s84, v56
	v_mbcnt_hi_u32_b32 v56, s85, v56
	s_add_i32 s77, s77, s32
	v_cndmask_b32_e64 v80, v80, v56, s[84:85]
	v_mov_b32_e32 v56, s77
	s_andn2_b64 s[84:85], s[14:15], s[12:13]
	v_mbcnt_lo_u32_b32 v56, s84, v56
	v_mbcnt_hi_u32_b32 v56, s85, v56
	s_nop 0
	v_cndmask_b32_e64 v80, v80, v56, s[84:85]
	s_and_b32 s83, s1, 0x4000
	s_add_i32 s99, s1, 0x2000
	s_and_b32 s99, s99, 0x6000
	v_mov_b32_e32 v112, s20
	v_mov_b32_e32 v113, s20
	v_mov_b32_e32 v114, s20
	v_mov_b32_e32 v115, s20
	s_add_i32 s101, s21, 8
	s_cmp_lt_u32 s101, s11
	s_cselect_b32 s101, 1, 0
	s_cmp_eq_u32 s100, s75
	s_cbranch_scc1 .Lbm_r1_pf
	s_lshl_b32 s32, s21, 2
	v_mov_b32_e32 v55, -1
	s_add_i32 s77, s32, 0
	v_cmp_eq_u32_e64 s[84:85], s77, v80
	s_nop 3
	s_and_b64 s[84:85], s[84:85], s[22:23]
	s_ff1_i32_b64 s77, s[84:85]
	v_writelane_b32 v55, s77, 0
	s_add_i32 s77, s32, 1
	v_cmp_eq_u32_e64 s[84:85], s77, v80
	s_nop 3
	s_and_b64 s[84:85], s[84:85], s[22:23]
	s_ff1_i32_b64 s77, s[84:85]
	v_writelane_b32 v55, s77, 1
	s_add_i32 s77, s32, 2
	v_cmp_eq_u32_e64 s[84:85], s77, v80
	s_nop 3
	s_and_b64 s[84:85], s[84:85], s[22:23]
	s_ff1_i32_b64 s77, s[84:85]
	v_writelane_b32 v55, s77, 2
	s_add_i32 s77, s32, 3
	v_cmp_eq_u32_e64 s[84:85], s77, v80
	s_nop 3
	s_and_b64 s[84:85], s[84:85], s[22:23]
	s_ff1_i32_b64 s77, s[84:85]
	v_writelane_b32 v55, s77, 3
	ds_bpermute_b32 v54, v250, v55
	s_waitcnt lgkmcnt(0)
	v_lshrrev_b32_e32 v56, 31, v54
	v_xor_b32_e32 v56, 1, v56
	v_mov_b32_e32 v79, v56
	v_max_i32_e32 v54, 0, v54
	v_lshlrev_b32_e32 v58, 11, v54
	v_mov_b32_e32 v59, 0
	v_lshl_add_u64 v[60:61], v[58:59], 0, v[246:247]
	global_load_dwordx4 v[104:107], v[60:61], off
	global_load_dwordx4 v[108:111], v[60:61], off offset:64
	v_lshl_add_u32 v63, v54, 4, v249
	ds_read_b32 v62, v63
	v_mul_u32_u24_e32 v83, 0x410, v54
	v_add_u32_e32 v83, v83, v248
	v_lshrrev_b64 v[58:59], v54, s[12:13]
	v_and_b32_e32 v58, v58, v56
	v_cmp_ne_u32_e32 vcc, 0, v58
	s_nop 1
	v_cndmask_b32_e32 v81, v2, v154, vcc
	s_cmp_lg_u64 vcc, 0
	s_cselect_b32 s21, 1, 0
	v_lshrrev_b64 v[58:59], v54, s[14:15]
	v_and_b32_e32 v58, v58, v56
	v_cmp_ne_u32_e32 vcc, 0, v58
	s_nop 1
	v_cndmask_b32_e32 v82, v2, v154, vcc
	s_cmp_lg_u64 vcc, 0
	s_cselect_b32 s32, 1, 0
	s_waitcnt lgkmcnt(0)
	v_sub_f32_e32 v81, v81, v62
	v_sub_f32_e32 v82, v82, v62
	s_waitcnt vmcnt(0)
	s_branch .Lbm_r1_go
.Lbm_r1_pf:
	v_mov_b32_e32 v54, v251
	v_lshrrev_b32_e32 v56, 31, v54
	v_xor_b32_e32 v56, 1, v56
	v_mov_b32_e32 v79, v56
	v_max_i32_e32 v54, 0, v54
	v_lshl_add_u32 v63, v54, 4, v249
	ds_read_b32 v62, v63
	v_mul_u32_u24_e32 v83, 0x410, v54
	v_add_u32_e32 v83, v83, v248
	v_lshrrev_b64 v[58:59], v54, s[12:13]
	v_and_b32_e32 v58, v58, v56
	v_cmp_ne_u32_e32 vcc, 0, v58
	s_nop 1
	v_cndmask_b32_e32 v81, v2, v154, vcc
	s_cmp_lg_u64 vcc, 0
	s_cselect_b32 s21, 1, 0
	v_lshrrev_b64 v[58:59], v54, s[14:15]
	v_and_b32_e32 v58, v58, v56
	v_cmp_ne_u32_e32 vcc, 0, v58
	s_nop 1
	v_cndmask_b32_e32 v82, v2, v154, vcc
	s_cmp_lg_u64 vcc, 0
	s_cselect_b32 s32, 1, 0
	s_waitcnt lgkmcnt(0)
	v_sub_f32_e32 v81, v81, v62
	v_sub_f32_e32 v82, v82, v62
	s_waitcnt vmcnt(4)
.Lbm_r1_go:
	s_cmp_eq_u32 s101, 1
	s_cbranch_scc1 .Lbm_r1_two
	s_and_b32 s77, s21, s32
	s_cmp_eq_u32 s77, 1
	s_cbranch_scc1 .Lbm_r1_full
	s_mov_b32 s77, s83
	s_cmp_eq_u32 s21, 1
	s_cbranch_scc1 .Lbm_r1_half
	s_mov_b32 s77, s99
	v_mov_b32_e32 v81, v82
.Lbm_r1_half:
	v_add_u32_e32 v148, s77, v192
	v_add_u32_e32 v149, v148, v195
	v_add_u32_e32 v148, v148, v193
	ds_read_b128 v[116:119], v148
	ds_read_b128 v[120:123], v149
	ds_read_b128 v[124:127], v148 offset:2048
	ds_read_b128 v[128:131], v149 offset:2048
	ds_read_b128 v[132:135], v148 offset:4096
	ds_read_b128 v[136:139], v149 offset:4096
	ds_read_b128 v[140:143], v148 offset:6144
	ds_read_b128 v[144:147], v149 offset:6144
	v_mov_b32_e32 v70, v81
	v_mov_b32_e32 v71, v81
	v_mov_b32_e32 v72, v81
	v_mov_b32_e32 v73, v81
	v_mov_b32_e32 v74, v81
	v_mov_b32_e32 v75, v81
	v_mov_b32_e32 v76, v81
	v_mov_b32_e32 v77, v81
	v_mov_b32_e32 v200, v81
	v_mov_b32_e32 v201, v81
	v_mov_b32_e32 v202, v81
	v_mov_b32_e32 v203, v81
	v_mov_b32_e32 v204, v81
	v_mov_b32_e32 v205, v81
	v_mov_b32_e32 v206, v81
	v_mov_b32_e32 v207, v81
	s_mov_b32 s83, -1
	s_add_i32 s77, s75, 2
	s_cmp_gt_i32 s77, s26
	s_cbranch_scc1 .Lbm_g1_end_h
	s_lshr_b32 s21, s77, 5
	v_mov_b32_e32 v255, v242
	s_cmp_eq_u32 s21, 1
	s_cselect_b64 vcc, -1, 0
	v_cndmask_b32_e32 v255, v255, v243, vcc
	s_cmp_eq_u32 s21, 2
	s_cselect_b64 vcc, -1, 0
	v_cndmask_b32_e32 v255, v255, v244, vcc
	s_cmp_eq_u32 s21, 3
	s_cselect_b64 vcc, -1, 0
	v_cndmask_b32_e32 v255, v255, v245, vcc
	s_and_b32 s21, s77, 31
	s_lshl_b32 s21, 1, s21
	s_lshl_b32 s32, s21, 1
	v_and_b32_e32 v80, s21, v255
	v_cmp_ne_u32_e64 s[12:13], 0, v80
	v_and_b32_e32 v80, s32, v255
	v_cmp_ne_u32_e64 s[14:15], 0, v80
	s_nop 3
	s_or_b64 s[22:23], s[12:13], s[14:15]
	s_bcnt1_i32_b64 s11, s[22:23]
	s_add_i32 s11, s11, 3
	s_lshr_b32 s11, s11, 2
	s_mov_b32 s21, s91
	s_cmp_ge_u32 s21, s11
	s_cbranch_scc1 .Lbm_g1_end_h
	s_add_i32 s83, s75, 2
; #define LAS __attribute__((address_space(3)))
; __device__ __forceinline__ float ex2(float x) { return __builtin_amdgcn_exp2f(x); }
; template <int C>
; __device__ __forceinline__ void attn_far1_fast(const LAS unsigned char* kb, const LAS unsigned char* vb, const bf16x8 (&qf)[2][2], int col, int q, float bias_far, bool sel, Softmax (&st)[2], f32x4 (&O)[2][4]) {
;     const f32x4 z4 = (f32x4){0.f, 0.f, 0.f, 0.f};
;     const float NEG = -__builtin_inff();
;     f32x4 S[4];
; #pragma unroll
;     for (int kt = 0; kt < 4; ++kt) { const bf16x8 k0 = lds_frag(kb, 16 * kt + col, q), k1 = lds_frag(kb, 16 * kt + col, 4 + q);
;         S[kt] = __builtin_amdgcn_mfma_f32_16x16x32_bf16(k0, qf[C][0], z4, 0, 0, 0); S[kt] = __builtin_amdgcn_mfma_f32_16x16x32_bf16(k1, qf[C][1], S[kt], 0, 0, 0); }
;     const float off = (sel ? bias_far : NEG) - st[C].m;
; #pragma unroll
;     for (int kt = 0; kt < 4; ++kt) { f32x4 p = S[kt] + off;
; #pragma unroll
;         for (int e = 0; e < 4; ++e) p[e] = ex2(p[e]);
;         S[kt] = p; }
;     const bf16x8 pf0 = pack8(S[0], S[1]), pf1 = pack8(S[2], S[3]);
;     st[C].l = __builtin_amdgcn_mfma_f32_16x16x32_bf16(ONES8, pf0, st[C].l, 0, 0, 0); st[C].l = __builtin_amdgcn_mfma_f32_16x16x32_bf16(ONES8, pf1, st[C].l, 0, 0, 0);
; #pragma unroll
;     for (int dt = 0; dt < 4; ++dt) { const bf16x8 vf0 = lds_frag(vb, 16 * dt + col, q), vf1 = lds_frag(vb, 16 * dt + col, 4 + q);
;         O[C][dt] = __builtin_amdgcn_mfma_f32_16x16x32_bf16(vf0, pf0, O[C][dt], 0, 0, 0); O[C][dt] = __builtin_amdgcn_mfma_f32_16x16x32_bf16(vf1, pf1, O[C][dt], 0, 0, 0); }
; }
.Lbm_g1_end_h:
	s_waitcnt lgkmcnt(6)
	v_mfma_f32_16x16x32_bf16 v[70:73], v[116:119], v[104:107], v[70:73]
	v_mfma_f32_16x16x32_bf16 v[70:73], v[120:123], v[108:111], v[70:73]
	s_waitcnt lgkmcnt(4)
	v_mfma_f32_16x16x32_bf16 v[74:77], v[124:127], v[104:107], v[74:77]
	v_mfma_f32_16x16x32_bf16 v[74:77], v[128:131], v[108:111], v[74:77]
	ds_read_b128 v[116:119], v148 offset:32768
	ds_read_b128 v[120:123], v149 offset:32768
	ds_read_b128 v[124:127], v148 offset:34816
	ds_read_b128 v[128:131], v149 offset:34816
	s_waitcnt lgkmcnt(6)
	v_mfma_f32_16x16x32_bf16 v[200:203], v[132:135], v[104:107], v[200:203]
	v_mfma_f32_16x16x32_bf16 v[200:203], v[136:139], v[108:111], v[200:203]
	s_waitcnt lgkmcnt(4)
	v_mfma_f32_16x16x32_bf16 v[204:207], v[140:143], v[104:107], v[204:207]
	v_mfma_f32_16x16x32_bf16 v[204:207], v[144:147], v[108:111], v[204:207]
	ds_read_b128 v[132:135], v148 offset:36864
	ds_read_b128 v[136:139], v149 offset:36864
	ds_read_b128 v[140:143], v148 offset:38912
	ds_read_b128 v[144:147], v149 offset:38912
	s_mov_b32 s100, -1
	s_cmp_lt_i32 s83, 0
	s_cbranch_scc1 .Lbm_g2_end_h
	s_andn2_b64 s[84:85], s[12:13], s[14:15]
	s_bcnt1_i32_b64 s77, s[84:85]
	v_mbcnt_lo_u32_b32 v80, s84, 0
	v_mbcnt_hi_u32_b32 v80, s85, v80
	v_mov_b32_e32 v255, s77
	s_and_b64 s[84:85], s[12:13], s[14:15]
	s_bcnt1_i32_b64 s32, s[84:85]
	v_mbcnt_lo_u32_b32 v255, s84, v255
	v_mbcnt_hi_u32_b32 v255, s85, v255
	s_add_i32 s77, s77, s32
	v_cndmask_b32_e64 v80, v80, v255, s[84:85]
	v_mov_b32_e32 v255, s77
	s_andn2_b64 s[84:85], s[14:15], s[12:13]
	v_mbcnt_lo_u32_b32 v255, s84, v255
	v_mbcnt_hi_u32_b32 v255, s85, v255
	s_nop 0
	v_cndmask_b32_e64 v80, v80, v255, s[84:85]
	s_mov_b32 s21, s91
	s_lshl_b32 s32, s21, 2
	v_mov_b32_e32 v199, -1
	s_add_i32 s77, s32, 0
	v_cmp_eq_u32_e64 s[84:85], s77, v80
	s_nop 3
	s_and_b64 s[84:85], s[84:85], s[22:23]
	s_ff1_i32_b64 s77, s[84:85]
	v_writelane_b32 v199, s77, 0
	s_add_i32 s77, s32, 1
	v_cmp_eq_u32_e64 s[84:85], s77, v80
	s_nop 3
	s_and_b64 s[84:85], s[84:85], s[22:23]
	s_ff1_i32_b64 s77, s[84:85]
	v_writelane_b32 v199, s77, 1
	s_add_i32 s77, s32, 2
	v_cmp_eq_u32_e64 s[84:85], s77, v80
	s_nop 3
	s_and_b64 s[84:85], s[84:85], s[22:23]
	s_ff1_i32_b64 s77, s[84:85]
	v_writelane_b32 v199, s77, 2
	s_add_i32 s77, s32, 3
	v_cmp_eq_u32_e64 s[84:85], s77, v80
	s_nop 3
	s_and_b64 s[84:85], s[84:85], s[22:23]
	s_ff1_i32_b64 s77, s[84:85]
	v_writelane_b32 v199, s77, 3
	ds_bpermute_b32 v251, v250, v199
	s_waitcnt lgkmcnt(0)
	v_max_i32_e32 v254, 0, v251
	v_lshlrev_b32_e32 v254, 11, v254
	v_mov_b32_e32 v255, 0
	v_lshl_add_u64 v[254:255], v[254:255], 0, v[246:247]
	global_load_dwordx4 v[104:107], v[254:255], off
	global_load_dwordx4 v[108:111], v[254:255], off offset:64
	s_mov_b32 s100, s83
.Lbm_g2_end_h:
	v_exp_f32_e32 v70, v70
	v_exp_f32_e32 v71, v71
	v_exp_f32_e32 v72, v72
	v_exp_f32_e32 v73, v73
	v_exp_f32_e32 v74, v74
	v_exp_f32_e32 v75, v75
	v_exp_f32_e32 v76, v76
	v_exp_f32_e32 v77, v77
	v_exp_f32_e32 v200, v200
	v_exp_f32_e32 v201, v201
	v_exp_f32_e32 v202, v202
	v_exp_f32_e32 v203, v203
	v_exp_f32_e32 v204, v204
	v_exp_f32_e32 v205, v205
	v_exp_f32_e32 v206, v206
	v_exp_f32_e32 v207, v207
	s_nop 0
	v_cvt_pk_bf16_f32 v70, v70, v71
	v_cvt_pk_bf16_f32 v71, v72, v73
	v_cvt_pk_bf16_f32 v72, v74, v75
	v_cvt_pk_bf16_f32 v73, v76, v77
	v_cvt_pk_bf16_f32 v74, v200, v201
	v_cvt_pk_bf16_f32 v75, v202, v203
	v_cvt_pk_bf16_f32 v76, v204, v205
	v_cvt_pk_bf16_f32 v77, v206, v207
	s_nop 1
	v_mfma_f32_16x16x32_bf16 v[100:103], v[112:115], v[70:73], 0
	v_mfma_f32_16x16x32_bf16 v[100:103], v[112:115], v[74:77], v[100:103]
	s_waitcnt lgkmcnt(4)
	v_mfma_f32_16x16x32_bf16 v[84:87], v[116:119], v[70:73], 0
	v_mfma_f32_16x16x32_bf16 v[84:87], v[120:123], v[74:77], v[84:87]
	v_mfma_f32_16x16x32_bf16 v[88:91], v[124:127], v[70:73], 0
	v_mfma_f32_16x16x32_bf16 v[88:91], v[128:131], v[74:77], v[88:91]
	v_lshlrev_b32_e32 v254, 6, v186
	v_sub_u32_e32 v254, v83, v254
	ds_read2_b32 v[200:201], v83 offset0:0 offset1:4
	ds_read2_b32 v[202:203], v83 offset0:8 offset1:12
	ds_read2_b32 v[204:205], v83 offset0:64 offset1:68
	ds_read2_b32 v[206:207], v83 offset0:72 offset1:76
	ds_read2_b32 v[62:63], v83 offset0:128 offset1:132
	ds_read2_b32 v[64:65], v83 offset0:136 offset1:140
	ds_read2_b32 v[66:67], v83 offset0:192 offset1:196
	ds_read2_b32 v[68:69], v83 offset0:200 offset1:204
	ds_read_b32 v199, v254 offset:1024
	s_waitcnt lgkmcnt(9)
	v_mfma_f32_16x16x32_bf16 v[92:95], v[132:135], v[70:73], 0
	v_mfma_f32_16x16x32_bf16 v[92:95], v[136:139], v[74:77], v[92:95]
	v_mfma_f32_16x16x32_bf16 v[96:99], v[140:143], v[70:73], 0
	v_mfma_f32_16x16x32_bf16 v[96:99], v[144:147], v[74:77], v[96:99]
	s_nop 1
	s_waitcnt lgkmcnt(0)
	v_add_f32_e32 v200, v200, v84
	v_add_f32_e32 v201, v201, v85
	v_add_f32_e32 v202, v202, v86
	v_add_f32_e32 v203, v203, v87
	v_add_f32_e32 v204, v204, v88
	v_add_f32_e32 v205, v205, v89
	v_add_f32_e32 v206, v206, v90
	v_add_f32_e32 v207, v207, v91
	v_add_f32_e32 v199, v199, v100
	v_add_f32_e32 v62, v62, v92
	v_add_f32_e32 v63, v63, v93
	v_add_f32_e32 v64, v64, v94
	v_add_f32_e32 v65, v65, v95
	v_add_f32_e32 v66, v66, v96
	v_add_f32_e32 v67, v67, v97
	v_add_f32_e32 v68, v68, v98
	v_add_f32_e32 v69, v69, v99
	v_cmp_ne_u32_e32 vcc, 0, v79
	s_and_saveexec_b64 s[84:85], vcc
	ds_write2_b32 v83, v200, v201 offset0:0 offset1:4
	ds_write2_b32 v83, v202, v203 offset0:8 offset1:12
	ds_write2_b32 v83, v204, v205 offset0:64 offset1:68
	ds_write2_b32 v83, v206, v207 offset0:72 offset1:76
	ds_write2_b32 v83, v62, v63 offset0:128 offset1:132
	ds_write2_b32 v83, v64, v65 offset0:136 offset1:140
	ds_write2_b32 v83, v66, v67 offset0:192 offset1:196
	ds_write2_b32 v83, v68, v69 offset0:200 offset1:204
	ds_write_b32 v254, v199 offset:1024
	s_mov_b64 exec, s[84:85]
	s_nop 3
	s_branch .Lbm_done
; #define LAS __attribute__((address_space(3)))
; __device__ __forceinline__ float ex2(float x) { return __builtin_amdgcn_exp2f(x); }
; template <bool SELMASK>
; __device__ __forceinline__ void attn_far_fast(const LAS unsigned char* kb, const LAS unsigned char* vb, const bf16x8 (&qf)[2][2], int col, int q, float bias_far, bool sel0, bool sel1, Softmax (&st)[2], f32x4 (&O)[2][4]) {
;     const f32x4 z4 = (f32x4){0.f, 0.f, 0.f, 0.f};
;     const float NEG = -__builtin_inff();
;     f32x4 S[2][4];
; #pragma unroll
;     for (int kt = 0; kt < 4; ++kt) { const bf16x8 k0 = lds_frag(kb, 16 * kt + col, q), k1 = lds_frag(kb, 16 * kt + col, 4 + q);
; #pragma unroll
;         for (int c = 0; c < 2; ++c) { S[c][kt] = __builtin_amdgcn_mfma_f32_16x16x32_bf16(k0, qf[c][0], z4, 0, 0, 0); S[c][kt] = __builtin_amdgcn_mfma_f32_16x16x32_bf16(k1, qf[c][1], S[c][kt], 0, 0, 0); } }
;     bf16x8 pf[2][2];
; #pragma unroll
;     for (int c = 0; c < 2; ++c) {
;         const bool sel = c == 0 ? sel0 : sel1;
;         const float off = ((SELMASK && !sel) ? NEG : bias_far) - st[c].m;
; #pragma unroll
;         for (int kt = 0; kt < 4; ++kt) { f32x4 p = S[c][kt] + off;
; #pragma unroll
;             for (int e = 0; e < 4; ++e) p[e] = ex2(p[e]);
;             S[c][kt] = p; }
;         pf[c][0] = pack8(S[c][0], S[c][1]); pf[c][1] = pack8(S[c][2], S[c][3]);
;         st[c].l = __builtin_amdgcn_mfma_f32_16x16x32_bf16(ONES8, pf[c][0], st[c].l, 0, 0, 0); st[c].l = __builtin_amdgcn_mfma_f32_16x16x32_bf16(ONES8, pf[c][1], st[c].l, 0, 0, 0);
;     }
.Lbm_r1_full:
	v_add_u32_e32 v148, s83, v192
	v_add_u32_e32 v149, v148, v195
	v_add_u32_e32 v148, v148, v193
	ds_read_b128 v[116:119], v148
	ds_read_b128 v[120:123], v149
	ds_read_b128 v[124:127], v148 offset:2048
	ds_read_b128 v[128:131], v149 offset:2048
	ds_read_b128 v[132:135], v148 offset:4096
	ds_read_b128 v[136:139], v149 offset:4096
	ds_read_b128 v[140:143], v148 offset:6144
	ds_read_b128 v[144:147], v149 offset:6144
	v_add_u32_e32 v208, s99, v192
	v_add_u32_e32 v209, v208, v195
	v_add_u32_e32 v208, v208, v193
	v_mov_b32_e32 v70, v81
	v_mov_b32_e32 v71, v81
	v_mov_b32_e32 v72, v81
	v_mov_b32_e32 v73, v81
	v_mov_b32_e32 v74, v81
	v_mov_b32_e32 v75, v81
	v_mov_b32_e32 v76, v81
	v_mov_b32_e32 v77, v81
	v_mov_b32_e32 v200, v81
	v_mov_b32_e32 v201, v81
	v_mov_b32_e32 v202, v81
	v_mov_b32_e32 v203, v81
	v_mov_b32_e32 v204, v81
	v_mov_b32_e32 v205, v81
	v_mov_b32_e32 v206, v81
	v_mov_b32_e32 v207, v81
	ds_read_b128 v[38:41], v208
	ds_read_b128 v[42:45], v209
	ds_read_b128 v[46:49], v208 offset:2048
	ds_read_b128 v[50:53], v209 offset:2048
	v_mov_b32_e32 v54, v82
	v_mov_b32_e32 v55, v82
	v_mov_b32_e32 v56, v82
	v_mov_b32_e32 v57, v82
	v_mov_b32_e32 v58, v82
	v_mov_b32_e32 v59, v82
	v_mov_b32_e32 v60, v82
	v_mov_b32_e32 v61, v82
	v_mov_b32_e32 v62, v82
	v_mov_b32_e32 v63, v82
	v_mov_b32_e32 v64, v82
	v_mov_b32_e32 v65, v82
	v_mov_b32_e32 v66, v82
	v_mov_b32_e32 v67, v82
	v_mov_b32_e32 v68, v82
	v_mov_b32_e32 v69, v82
	s_mov_b32 s83, -1
	s_add_i32 s77, s75, 2
	s_cmp_gt_i32 s77, s26
	s_cbranch_scc1 .Lbm_g1_end_a
	s_lshr_b32 s21, s77, 5
	v_mov_b32_e32 v255, v242
	s_cmp_eq_u32 s21, 1
	s_cselect_b64 vcc, -1, 0
	v_cndmask_b32_e32 v255, v255, v243, vcc
	s_cmp_eq_u32 s21, 2
	s_cselect_b64 vcc, -1, 0
	v_cndmask_b32_e32 v255, v255, v244, vcc
	s_cmp_eq_u32 s21, 3
	s_cselect_b64 vcc, -1, 0
	v_cndmask_b32_e32 v255, v255, v245, vcc
	s_and_b32 s21, s77, 31
	s_lshl_b32 s21, 1, s21
	s_lshl_b32 s32, s21, 1
	v_and_b32_e32 v80, s21, v255
	v_cmp_ne_u32_e64 s[12:13], 0, v80
	v_and_b32_e32 v80, s32, v255
	v_cmp_ne_u32_e64 s[14:15], 0, v80
	s_nop 3
	s_or_b64 s[22:23], s[12:13], s[14:15]
	s_bcnt1_i32_b64 s11, s[22:23]
	s_add_i32 s11, s11, 3
	s_lshr_b32 s11, s11, 2
	s_mov_b32 s21, s91
	s_cmp_ge_u32 s21, s11
	s_cbranch_scc1 .Lbm_g1_end_a
	s_add_i32 s83, s75, 2
.Lbm_g1_end_a:
	s_waitcnt lgkmcnt(10)
	v_mfma_f32_16x16x32_bf16 v[70:73], v[116:119], v[104:107], v[70:73]
	v_mfma_f32_16x16x32_bf16 v[70:73], v[120:123], v[108:111], v[70:73]
	s_waitcnt lgkmcnt(8)
	v_mfma_f32_16x16x32_bf16 v[74:77], v[124:127], v[104:107], v[74:77]
	v_mfma_f32_16x16x32_bf16 v[74:77], v[128:131], v[108:111], v[74:77]
	ds_read_b128 v[116:119], v148 offset:32768
	ds_read_b128 v[120:123], v149 offset:32768
	ds_read_b128 v[124:127], v148 offset:34816
	ds_read_b128 v[128:131], v149 offset:34816
	s_waitcnt lgkmcnt(10)
	v_mfma_f32_16x16x32_bf16 v[200:203], v[132:135], v[104:107], v[200:203]
	v_mfma_f32_16x16x32_bf16 v[200:203], v[136:139], v[108:111], v[200:203]
	s_waitcnt lgkmcnt(8)
	v_mfma_f32_16x16x32_bf16 v[204:207], v[140:143], v[104:107], v[204:207]
	v_mfma_f32_16x16x32_bf16 v[204:207], v[144:147], v[108:111], v[204:207]
	ds_read_b128 v[132:135], v148 offset:36864
	ds_read_b128 v[136:139], v149 offset:36864
	ds_read_b128 v[140:143], v148 offset:38912
	ds_read_b128 v[144:147], v149 offset:38912
	s_waitcnt lgkmcnt(10)
	v_mfma_f32_16x16x32_bf16 v[54:57], v[38:41], v[104:107], v[54:57]
	v_mfma_f32_16x16x32_bf16 v[54:57], v[42:45], v[108:111], v[54:57]
	s_waitcnt lgkmcnt(8)
	v_mfma_f32_16x16x32_bf16 v[58:61], v[46:49], v[104:107], v[58:61]
	v_mfma_f32_16x16x32_bf16 v[58:61], v[50:53], v[108:111], v[58:61]
	ds_read_b128 v[38:41], v208 offset:4096
	ds_read_b128 v[42:45], v209 offset:4096
	ds_read_b128 v[46:49], v208 offset:6144
	ds_read_b128 v[50:53], v209 offset:6144
	s_cmp_lt_i32 s83, 0
	s_cbranch_scc1 .Lbm_g2_end_a
	s_andn2_b64 s[84:85], s[12:13], s[14:15]
	s_bcnt1_i32_b64 s77, s[84:85]
	v_mbcnt_lo_u32_b32 v80, s84, 0
	v_mbcnt_hi_u32_b32 v80, s85, v80
	v_mov_b32_e32 v255, s77
	s_and_b64 s[84:85], s[12:13], s[14:15]
	s_bcnt1_i32_b64 s32, s[84:85]
	v_mbcnt_lo_u32_b32 v255, s84, v255
	v_mbcnt_hi_u32_b32 v255, s85, v255
	s_add_i32 s77, s77, s32
	v_cndmask_b32_e64 v80, v80, v255, s[84:85]
	v_mov_b32_e32 v255, s77
	s_andn2_b64 s[84:85], s[14:15], s[12:13]
	v_mbcnt_lo_u32_b32 v255, s84, v255
	v_mbcnt_hi_u32_b32 v255, s85, v255
	s_nop 0
	v_cndmask_b32_e64 v80, v80, v255, s[84:85]
	s_mov_b32 s21, s91
	s_lshl_b32 s32, s21, 2
	v_mov_b32_e32 v199, -1
	s_add_i32 s77, s32, 0
	v_cmp_eq_u32_e64 s[84:85], s77, v80
	s_nop 3
	s_and_b64 s[84:85], s[84:85], s[22:23]
	s_ff1_i32_b64 s77, s[84:85]
	v_writelane_b32 v199, s77, 0
	s_add_i32 s77, s32, 1
	v_cmp_eq_u32_e64 s[84:85], s77, v80
	s_nop 3
	s_and_b64 s[84:85], s[84:85], s[22:23]
	s_ff1_i32_b64 s77, s[84:85]
	v_writelane_b32 v199, s77, 1
	s_add_i32 s77, s32, 2
	v_cmp_eq_u32_e64 s[84:85], s77, v80
	s_nop 3
	s_and_b64 s[84:85], s[84:85], s[22:23]
	s_ff1_i32_b64 s77, s[84:85]
	v_writelane_b32 v199, s77, 2
	s_add_i32 s77, s32, 3
	v_cmp_eq_u32_e64 s[84:85], s77, v80
	s_nop 3
	s_and_b64 s[84:85], s[84:85], s[22:23]
	s_ff1_i32_b64 s77, s[84:85]
	v_writelane_b32 v199, s77, 3
	ds_bpermute_b32 v251, v250, v199
	s_waitcnt lgkmcnt(0)

; __device__ __forceinline__ float ex2(float x) { return __builtin_amdgcn_exp2f(x); }
; template <bool SELMASK>
; __device__ __forceinline__ void attn_far_fast(const LAS unsigned char* kb, const LAS unsigned char* vb, const bf16x8 (&qf)[2][2], int col, int q, float bias_far, bool sel0, bool sel1, Softmax (&st)[2], f32x4 (&O)[2][4]) {
;     ...
;     bf16x8 pf[2][2];
; #pragma unroll
;     for (int c = 0; c < 2; ++c) {
;         const bool sel = c == 0 ? sel0 : sel1;
;         const float off = ((SELMASK && !sel) ? NEG : bias_far) - st[c].m;
; #pragma unroll
;         for (int kt = 0; kt < 4; ++kt) { f32x4 p = S[c][kt] + off;
; #pragma unroll
;             for (int e = 0; e < 4; ++e) p[e] = ex2(p[e]);
;             S[c][kt] = p; }
;         pf[c][0] = pack8(S[c][0], S[c][1]); pf[c][1] = pack8(S[c][2], S[c][3]);
;         st[c].l = __builtin_amdgcn_mfma_f32_16x16x32_bf16(ONES8, pf[c][0], st[c].l, 0, 0, 0); st[c].l = __builtin_amdgcn_mfma_f32_16x16x32_bf16(ONES8, pf[c][1], st[c].l, 0, 0, 0);
;     }
; #pragma unroll
;     for (int c32 = 0; c32 < 2; ++c32)
; #pragma unroll
;         for (int dt = 0; dt < 4; ++dt) { const bf16x8 vf = lds_frag(vb, 16 * dt + col, 4 * c32 + q);
;             O[0][dt] = __builtin_amdgcn_mfma_f32_16x16x32_bf16(vf, pf[0][c32], O[0][dt], 0, 0, 0);
;             O[1][dt] = __builtin_amdgcn_mfma_f32_16x16x32_bf16(vf, pf[1][c32], O[1][dt], 0, 0, 0); }
.Lbm_pi_end_a:
	v_exp_f32_e32 v54, v54
	v_exp_f32_e32 v55, v55
	v_exp_f32_e32 v56, v56
	v_exp_f32_e32 v57, v57
	v_exp_f32_e32 v58, v58
	v_exp_f32_e32 v59, v59
	v_exp_f32_e32 v60, v60
	v_exp_f32_e32 v61, v61
	v_exp_f32_e32 v62, v62
	v_exp_f32_e32 v63, v63
	v_exp_f32_e32 v64, v64
	v_exp_f32_e32 v65, v65
	v_exp_f32_e32 v66, v66
	v_exp_f32_e32 v67, v67
	v_exp_f32_e32 v68, v68
	v_exp_f32_e32 v69, v69
	s_nop 0
	v_cvt_pk_bf16_f32 v54, v54, v55
	v_cvt_pk_bf16_f32 v55, v56, v57
	v_cvt_pk_bf16_f32 v56, v58, v59
	v_cvt_pk_bf16_f32 v57, v60, v61
	v_cvt_pk_bf16_f32 v58, v62, v63
	v_cvt_pk_bf16_f32 v59, v64, v65
	v_cvt_pk_bf16_f32 v60, v66, v67
	v_cvt_pk_bf16_f32 v61, v68, v69
	s_nop 1
	v_mfma_f32_16x16x32_bf16 v[100:103], v[112:115], v[54:57], v[100:103]
	v_mfma_f32_16x16x32_bf16 v[100:103], v[112:115], v[58:61], v[100:103]
	s_waitcnt lgkmcnt(4)
	v_mfma_f32_16x16x32_bf16 v[84:87], v[116:119], v[54:57], v[84:87]
	v_mfma_f32_16x16x32_bf16 v[84:87], v[120:123], v[58:61], v[84:87]
	v_mfma_f32_16x16x32_bf16 v[88:91], v[124:127], v[54:57], v[88:91]
	v_mfma_f32_16x16x32_bf16 v[88:91], v[128:131], v[58:61], v[88:91]
	v_lshlrev_b32_e32 v254, 6, v186
	v_sub_u32_e32 v254, v83, v254
	ds_read2_b32 v[200:201], v83 offset0:0 offset1:4
	ds_read2_b32 v[202:203], v83 offset0:8 offset1:12
	ds_read2_b32 v[204:205], v83 offset0:64 offset1:68
	ds_read2_b32 v[206:207], v83 offset0:72 offset1:76
	ds_read2_b32 v[62:63], v83 offset0:128 offset1:132
	ds_read2_b32 v[64:65], v83 offset0:136 offset1:140
	ds_read2_b32 v[66:67], v83 offset0:192 offset1:196
	ds_read2_b32 v[68:69], v83 offset0:200 offset1:204
	ds_read_b32 v199, v254 offset:1024
	s_waitcnt lgkmcnt(9)
	v_mfma_f32_16x16x32_bf16 v[92:95], v[132:135], v[54:57], v[92:95]
	v_mfma_f32_16x16x32_bf16 v[92:95], v[136:139], v[58:61], v[92:95]
	v_mfma_f32_16x16x32_bf16 v[96:99], v[140:143], v[54:57], v[96:99]
	v_mfma_f32_16x16x32_bf16 v[96:99], v[144:147], v[58:61], v[96:99]
	s_nop 1
	s_waitcnt lgkmcnt(0)
	v_add_f32_e32 v200, v200, v84
	v_add_f32_e32 v201, v201, v85
	v_add_f32_e32 v202, v202, v86
	v_add_f32_e32 v203, v203, v87
	v_add_f32_e32 v204, v204, v88
	v_add_f32_e32 v205, v205, v89
	v_add_f32_e32 v206, v206, v90
	v_add_f32_e32 v207, v207, v91
	v_add_f32_e32 v199, v199, v100
	v_add_f32_e32 v62, v62, v92
	v_add_f32_e32 v63, v63, v93
	v_add_f32_e32 v64, v64, v94
	v_add_f32_e32 v65, v65, v95
	v_add_f32_e32 v66, v66, v96
	v_add_f32_e32 v67, v67, v97
	v_add_f32_e32 v68, v68, v98
	v_add_f32_e32 v69, v69, v99
	v_cmp_ne_u32_e32 vcc, 0, v79
	s_and_saveexec_b64 s[84:85], vcc
	ds_write2_b32 v83, v200, v201 offset0:0 offset1:4
	ds_write2_b32 v83, v202, v203 offset0:8 offset1:12
	ds_write2_b32 v83, v204, v205 offset0:64 offset1:68
	ds_write2_b32 v83, v206, v207 offset0:72 offset1:76
	ds_write2_b32 v83, v62, v63 offset0:128 offset1:132
	ds_write2_b32 v83, v64, v65 offset0:136 offset1:140
	ds_write2_b32 v83, v66, v67 offset0:192 offset1:196
	ds_write2_b32 v83, v68, v69 offset0:200 offset1:204
	ds_write_b32 v254, v199 offset:1024
	s_mov_b64 exec, s[84:85]
	s_nop 3
	s_branch .Lbm_done
.Lbm_r1_two:
	v_add_u32_e32 v148, s83, v192
	v_add_u32_e32 v149, v148, v195
	v_add_u32_e32 v148, v148, v193
	ds_read_b128 v[116:119], v148
	ds_read_b128 v[120:123], v149
	ds_read_b128 v[124:127], v148 offset:2048
	ds_read_b128 v[128:131], v149 offset:2048
	ds_read_b128 v[132:135], v148 offset:4096
	ds_read_b128 v[136:139], v149 offset:4096
	ds_read_b128 v[140:143], v148 offset:6144
	ds_read_b128 v[144:147], v149 offset:6144
	v_add_u32_e32 v208, s99, v192
	v_add_u32_e32 v209, v208, v195
	v_add_u32_e32 v208, v208, v193
	v_mov_b32_e32 v70, v81
	v_mov_b32_e32 v71, v81
	v_mov_b32_e32 v72, v81
	v_mov_b32_e32 v73, v81
	v_mov_b32_e32 v74, v81
	v_mov_b32_e32 v75, v81
	v_mov_b32_e32 v76, v81
	v_mov_b32_e32 v77, v81
	v_mov_b32_e32 v200, v81
	v_mov_b32_e32 v201, v81
	v_mov_b32_e32 v202, v81
	v_mov_b32_e32 v203, v81
	v_mov_b32_e32 v204, v81
	v_mov_b32_e32 v205, v81
	v_mov_b32_e32 v206, v81
	v_mov_b32_e32 v207, v81
	ds_read_b128 v[38:41], v208
	ds_read_b128 v[42:45], v209
	ds_read_b128 v[46:49], v208 offset:2048
	ds_read_b128 v[50:53], v209 offset:2048
	v_mov_b32_e32 v54, v82
	v_mov_b32_e32 v55, v82
	v_mov_b32_e32 v56, v82
	v_mov_b32_e32 v57, v82
	v_mov_b32_e32 v58, v82
	v_mov_b32_e32 v59, v82
	v_mov_b32_e32 v60, v82
	v_mov_b32_e32 v61, v82
	v_mov_b32_e32 v62, v82
	v_mov_b32_e32 v63, v82
	v_mov_b32_e32 v64, v82
	v_mov_b32_e32 v65, v82
	v_mov_b32_e32 v66, v82
	v_mov_b32_e32 v67, v82
	v_mov_b32_e32 v68, v82
	v_mov_b32_e32 v69, v82
	s_waitcnt lgkmcnt(10)
	v_mfma_f32_16x16x32_bf16 v[70:73], v[116:119], v[104:107], v[70:73]
	v_mfma_f32_16x16x32_bf16 v[70:73], v[120:123], v[108:111], v[70:73]
	s_waitcnt lgkmcnt(8)
	v_mfma_f32_16x16x32_bf16 v[74:77], v[124:127], v[104:107], v[74:77]
	v_mfma_f32_16x16x32_bf16 v[74:77], v[128:131], v[108:111], v[74:77]
	ds_read_b128 v[116:119], v148 offset:32768
	ds_read_b128 v[120:123], v149 offset:32768
	ds_read_b128 v[124:127], v148 offset:34816
	ds_read_b128 v[128:131], v149 offset:34816
	s_waitcnt lgkmcnt(10)
	v_mfma_f32_16x16x32_bf16 v[200:203], v[132:135], v[104:107], v[200:203]
	v_mfma_f32_16x16x32_bf16 v[200:203], v[136:139], v[108:111], v[200:203]
	s_waitcnt lgkmcnt(8)
	v_mfma_f32_16x16x32_bf16 v[204:207], v[140:143], v[104:107], v[204:207]
	v_mfma_f32_16x16x32_bf16 v[204:207], v[144:147], v[108:111], v[204:207]
	ds_read_b128 v[132:135], v148 offset:36864
	ds_read_b128 v[136:139], v149 offset:36864
	ds_read_b128 v[140:143], v148 offset:38912
	ds_read_b128 v[144:147], v149 offset:38912
	s_waitcnt lgkmcnt(10)
	v_mfma_f32_16x16x32_bf16 v[54:57], v[38:41], v[104:107], v[54:57]
	v_mfma_f32_16x16x32_bf16 v[54:57], v[42:45], v[108:111], v[54:57]
	s_waitcnt lgkmcnt(8)
; #define LAS __attribute__((address_space(3)))
; __device__ __forceinline__ float ex2(float x) { return __builtin_amdgcn_exp2f(x); }
; template <bool SELMASK>
; __device__ __forceinline__ void attn_far_fast(const LAS unsigned char* kb, const LAS unsigned char* vb, const bf16x8 (&qf)[2][2], int col, int q, float bias_far, bool sel0, bool sel1, Softmax (&st)[2], f32x4 (&O)[2][4]) {
;     const f32x4 z4 = (f32x4){0.f, 0.f, 0.f, 0.f};
;     const float NEG = -__builtin_inff();
;     f32x4 S[2][4];
; #pragma unroll
;     for (int kt = 0; kt < 4; ++kt) { const bf16x8 k0 = lds_frag(kb, 16 * kt + col, q), k1 = lds_frag(kb, 16 * kt + col, 4 + q);
; #pragma unroll
;         for (int c = 0; c < 2; ++c) { S[c][kt] = __builtin_amdgcn_mfma_f32_16x16x32_bf16(k0, qf[c][0], z4, 0, 0, 0); S[c][kt] = __builtin_amdgcn_mfma_f32_16x16x32_bf16(k1, qf[c][1], S[c][kt], 0, 0, 0); } }
;     bf16x8 pf[2][2];
; #pragma unroll
;     for (int c = 0; c < 2; ++c) {
;         const bool sel = c == 0 ? sel0 : sel1;
;         const float off = ((SELMASK && !sel) ? NEG : bias_far) - st[c].m;
; #pragma unroll
;         for (int kt = 0; kt < 4; ++kt) { f32x4 p = S[c][kt] + off;
; #pragma unroll
;             for (int e = 0; e < 4; ++e) p[e] = ex2(p[e]);
;             S[c][kt] = p; }
;         pf[c][0] = pack8(S[c][0], S[c][1]); pf[c][1] = pack8(S[c][2], S[c][3]);
;         st[c].l = __builtin_amdgcn_mfma_f32_16x16x32_bf16(ONES8, pf[c][0], st[c].l, 0, 0, 0); st[c].l = __builtin_amdgcn_mfma_f32_16x16x32_bf16(ONES8, pf[c][1], st[c].l, 0, 0, 0);
;     }
; #pragma unroll
;     for (int c32 = 0; c32 < 2; ++c32)
; #pragma unroll
;         for (int dt = 0; dt < 4; ++dt) { const bf16x8 vf = lds_frag(vb, 16 * dt + col, 4 * c32 + q);
;             O[0][dt] = __builtin_amdgcn_mfma_f32_16x16x32_bf16(vf, pf[0][c32], O[0][dt], 0, 0, 0);
;             O[1][dt] = __builtin_amdgcn_mfma_f32_16x16x32_bf16(vf, pf[1][c32], O[1][dt], 0, 0, 0); }
	v_mfma_f32_16x16x32_bf16 v[58:61], v[46:49], v[104:107], v[58:61]
	v_mfma_f32_16x16x32_bf16 v[58:61], v[50:53], v[108:111], v[58:61]
	ds_read_b128 v[38:41], v208 offset:4096
	ds_read_b128 v[42:45], v209 offset:4096
	ds_read_b128 v[46:49], v208 offset:6144
	ds_read_b128 v[50:53], v209 offset:6144
	v_exp_f32_e32 v70, v70
	v_exp_f32_e32 v71, v71
	v_exp_f32_e32 v72, v72
	v_exp_f32_e32 v73, v73
	v_exp_f32_e32 v74, v74
	v_exp_f32_e32 v75, v75
	v_exp_f32_e32 v76, v76
	v_exp_f32_e32 v77, v77
	v_exp_f32_e32 v200, v200
	v_exp_f32_e32 v201, v201
	v_exp_f32_e32 v202, v202
	v_exp_f32_e32 v203, v203
	v_exp_f32_e32 v204, v204
	v_exp_f32_e32 v205, v205
	v_exp_f32_e32 v206, v206
	v_exp_f32_e32 v207, v207
	s_nop 0
	v_cvt_pk_bf16_f32 v70, v70, v71
	v_cvt_pk_bf16_f32 v71, v72, v73
	v_cvt_pk_bf16_f32 v72, v74, v75
	v_cvt_pk_bf16_f32 v73, v76, v77
	v_cvt_pk_bf16_f32 v74, v200, v201
	v_cvt_pk_bf16_f32 v75, v202, v203
	v_cvt_pk_bf16_f32 v76, v204, v205
	v_cvt_pk_bf16_f32 v77, v206, v207
	s_nop 1
	v_mfma_f32_16x16x32_bf16 v[100:103], v[112:115], v[70:73], 0
	v_mfma_f32_16x16x32_bf16 v[100:103], v[112:115], v[74:77], v[100:103]
	s_waitcnt lgkmcnt(4)
	v_mfma_f32_16x16x32_bf16 v[84:87], v[116:119], v[70:73], 0
	v_mfma_f32_16x16x32_bf16 v[84:87], v[120:123], v[74:77], v[84:87]
	v_mfma_f32_16x16x32_bf16 v[88:91], v[124:127], v[70:73], 0
	v_mfma_f32_16x16x32_bf16 v[88:91], v[128:131], v[74:77], v[88:91]
	v_mfma_f32_16x16x32_bf16 v[92:95], v[132:135], v[70:73], 0
	v_mfma_f32_16x16x32_bf16 v[92:95], v[136:139], v[74:77], v[92:95]
	v_mfma_f32_16x16x32_bf16 v[96:99], v[140:143], v[70:73], 0
	v_mfma_f32_16x16x32_bf16 v[96:99], v[144:147], v[74:77], v[96:99]
	s_waitcnt lgkmcnt(2)
	v_mfma_f32_16x16x32_bf16 v[62:65], v[38:41], v[104:107], v[62:65]
	v_mfma_f32_16x16x32_bf16 v[62:65], v[42:45], v[108:111], v[62:65]
	s_waitcnt lgkmcnt(0)
	v_mfma_f32_16x16x32_bf16 v[66:69], v[46:49], v[104:107], v[66:69]
	v_mfma_f32_16x16x32_bf16 v[66:69], v[50:53], v[108:111], v[66:69]
	ds_read_b128 v[116:119], v208 offset:32768
	ds_read_b128 v[120:123], v209 offset:32768
	ds_read_b128 v[124:127], v208 offset:34816
	ds_read_b128 v[128:131], v209 offset:34816
	ds_read_b128 v[132:135], v208 offset:36864
	ds_read_b128 v[136:139], v209 offset:36864
	ds_read_b128 v[140:143], v208 offset:38912
	ds_read_b128 v[144:147], v209 offset:38912
	s_nop 3
	v_exp_f32_e32 v54, v54
	v_exp_f32_e32 v55, v55
	v_exp_f32_e32 v56, v56
	v_exp_f32_e32 v57, v57
	v_exp_f32_e32 v58, v58
	v_exp_f32_e32 v59, v59
	v_exp_f32_e32 v60, v60
	v_exp_f32_e32 v61, v61
	v_exp_f32_e32 v62, v62
	v_exp_f32_e32 v63, v63
	v_exp_f32_e32 v64, v64
	v_exp_f32_e32 v65, v65
	v_exp_f32_e32 v66, v66
	v_exp_f32_e32 v67, v67
	v_exp_f32_e32 v68, v68
	v_exp_f32_e32 v69, v69
	s_nop 0
	v_cvt_pk_bf16_f32 v54, v54, v55
	v_cvt_pk_bf16_f32 v55, v56, v57
	v_cvt_pk_bf16_f32 v56, v58, v59
	v_cvt_pk_bf16_f32 v57, v60, v61
	v_cvt_pk_bf16_f32 v58, v62, v63
	v_cvt_pk_bf16_f32 v59, v64, v65
	v_cvt_pk_bf16_f32 v60, v66, v67
	v_cvt_pk_bf16_f32 v61, v68, v69
	s_nop 1
	v_mfma_f32_16x16x32_bf16 v[100:103], v[112:115], v[54:57], v[100:103]
	v_mfma_f32_16x16x32_bf16 v[100:103], v[112:115], v[58:61], v[100:103]
	s_waitcnt lgkmcnt(4)
	v_mfma_f32_16x16x32_bf16 v[84:87], v[116:119], v[54:57], v[84:87]
	v_mfma_f32_16x16x32_bf16 v[84:87], v[120:123], v[58:61], v[84:87]
	v_mfma_f32_16x16x32_bf16 v[88:91], v[124:127], v[54:57], v[88:91]
	v_mfma_f32_16x16x32_bf16 v[88:91], v[128:131], v[58:61], v[88:91]
	v_lshlrev_b32_e32 v254, 6, v186
	v_sub_u32_e32 v254, v83, v254
	ds_read2_b32 v[200:201], v83 offset0:0 offset1:4
	ds_read2_b32 v[202:203], v83 offset0:8 offset1:12
	ds_read2_b32 v[204:205], v83 offset0:64 offset1:68
	ds_read2_b32 v[206:207], v83 offset0:72 offset1:76
	ds_read2_b32 v[62:63], v83 offset0:128 offset1:132
	ds_read2_b32 v[64:65], v83 offset0:136 offset1:140
	ds_read2_b32 v[66:67], v83 offset0:192 offset1:196
	ds_read2_b32 v[68:69], v83 offset0:200 offset1:204
	ds_read_b32 v199, v254 offset:1024
	s_waitcnt lgkmcnt(9)
	v_mfma_f32_16x16x32_bf16 v[92:95], v[132:135], v[54:57], v[92:95]
	v_mfma_f32_16x16x32_bf16 v[92:95], v[136:139], v[58:61], v[92:95]
	v_mfma_f32_16x16x32_bf16 v[96:99], v[140:143], v[54:57], v[96:99]
	v_mfma_f32_16x16x32_bf16 v[96:99], v[144:147], v[58:61], v[96:99]
	s_nop 1
	s_waitcnt lgkmcnt(0)
	v_add_f32_e32 v200, v200, v84
	v_add_f32_e32 v201, v201, v85
	v_add_f32_e32 v202, v202, v86
	v_add_f32_e32 v203, v203, v87
	v_add_f32_e32 v204, v204, v88
	v_add_f32_e32 v205, v205, v89
	v_add_f32_e32 v206, v206, v90
	v_add_f32_e32 v207, v207, v91
	v_add_f32_e32 v199, v199, v100
	v_add_f32_e32 v62, v62, v92
	v_add_f32_e32 v63, v63, v93
	v_add_f32_e32 v64, v64, v94
	v_add_f32_e32 v65, v65, v95
	v_add_f32_e32 v66, v66, v96
	v_add_f32_e32 v67, v67, v97
	v_add_f32_e32 v68, v68, v98
	v_add_f32_e32 v69, v69, v99
	v_cmp_ne_u32_e32 vcc, 0, v79
	s_and_saveexec_b64 s[84:85], vcc
	ds_write2_b32 v83, v200, v201 offset0:0 offset1:4
	ds_write2_b32 v83, v202, v203 offset0:8 offset1:12
	ds_write2_b32 v83, v204, v205 offset0:64 offset1:68
	ds_write2_b32 v83, v206, v207 offset0:72 offset1:76
	ds_write2_b32 v83, v62, v63 offset0:128 offset1:132
	ds_write2_b32 v83, v64, v65 offset0:136 offset1:140
	ds_write2_b32 v83, v66, v67 offset0:192 offset1:196
	ds_write2_b32 v83, v68, v69 offset0:200 offset1:204
	ds_write_b32 v254, v199 offset:1024
	s_mov_b64 exec, s[84:85]
	s_nop 3
	s_mov_b32 s100, -1
	s_mov_b32 s21, s91
	s_add_i32 s21, s21, 8
	s_lshl_b32 s32, s21, 2
	v_mov_b32_e32 v55, -1
	s_add_i32 s77, s32, 0
	v_cmp_eq_u32_e64 s[84:85], s77, v80
	s_nop 3
	s_and_b64 s[84:85], s[84:85], s[22:23]
	s_ff1_i32_b64 s77, s[84:85]
	v_writelane_b32 v55, s77, 0
	s_add_i32 s77, s32, 1
	v_cmp_eq_u32_e64 s[84:85], s77, v80
	s_nop 3
	s_and_b64 s[84:85], s[84:85], s[22:23]
	s_ff1_i32_b64 s77, s[84:85]
	v_writelane_b32 v55, s77, 1
	s_add_i32 s77, s32, 2
	v_cmp_eq_u32_e64 s[84:85], s77, v80
	s_nop 3
	s_and_b64 s[84:85], s[84:85], s[22:23]
	s_ff1_i32_b64 s77, s[84:85]
	v_writelane_b32 v55, s77, 2
	s_add_i32 s77, s32, 3
	v_cmp_eq_u32_e64 s[84:85], s77, v80
	s_nop 3
	s_and_b64 s[84:85], s[84:85], s[22:23]
	s_ff1_i32_b64 s77, s[84:85]
	v_writelane_b32 v55, s77, 3
	ds_bpermute_b32 v54, v250, v55
	s_waitcnt lgkmcnt(0)
; #define LAS __attribute__((address_space(3)))
; __device__ __forceinline__ float ex2(float x) { return __builtin_amdgcn_exp2f(x); }
; template <bool SELMASK>
; __device__ __forceinline__ void attn_far_fast(const LAS unsigned char* kb, const LAS unsigned char* vb, const bf16x8 (&qf)[2][2], int col, int q, float bias_far, bool sel0, bool sel1, Softmax (&st)[2], f32x4 (&O)[2][4]) {
;     const f32x4 z4 = (f32x4){0.f, 0.f, 0.f, 0.f};
;     const float NEG = -__builtin_inff();
;     f32x4 S[2][4];
; #pragma unroll
;     for (int kt = 0; kt < 4; ++kt) { const bf16x8 k0 = lds_frag(kb, 16 * kt + col, q), k1 = lds_frag(kb, 16 * kt + col, 4 + q);
; #pragma unroll
;         for (int c = 0; c < 2; ++c) { S[c][kt] = __builtin_amdgcn_mfma_f32_16x16x32_bf16(k0, qf[c][0], z4, 0, 0, 0); S[c][kt] = __builtin_amdgcn_mfma_f32_16x16x32_bf16(k1, qf[c][1], S[c][kt], 0, 0, 0); } }
;     bf16x8 pf[2][2];
; #pragma unroll
;     for (int c = 0; c < 2; ++c) {
;         const bool sel = c == 0 ? sel0 : sel1;
;         const float off = ((SELMASK && !sel) ? NEG : bias_far) - st[c].m;
; #pragma unroll
;         for (int kt = 0; kt < 4; ++kt) { f32x4 p = S[c][kt] + off;
; #pragma unroll
;             for (int e = 0; e < 4; ++e) p[e] = ex2(p[e]);
;             S[c][kt] = p; }
;         pf[c][0] = pack8(S[c][0], S[c][1]); pf[c][1] = pack8(S[c][2], S[c][3]);
;         st[c].l = __builtin_amdgcn_mfma_f32_16x16x32_bf16(ONES8, pf[c][0], st[c].l, 0, 0, 0); st[c].l = __builtin_amdgcn_mfma_f32_16x16x32_bf16(ONES8, pf[c][1], st[c].l, 0, 0, 0);
;     }
	v_lshrrev_b32_e32 v56, 31, v54
	v_xor_b32_e32 v56, 1, v56
	v_mov_b32_e32 v79, v56
	v_max_i32_e32 v54, 0, v54
	v_lshlrev_b32_e32 v58, 11, v54
	v_mov_b32_e32 v59, 0
	v_lshl_add_u64 v[60:61], v[58:59], 0, v[246:247]
	global_load_dwordx4 v[104:107], v[60:61], off
	global_load_dwordx4 v[108:111], v[60:61], off offset:64
	v_lshl_add_u32 v63, v54, 4, v249
	ds_read_b32 v62, v63
	v_mul_u32_u24_e32 v83, 0x410, v54
	v_add_u32_e32 v83, v83, v248
	v_lshrrev_b64 v[58:59], v54, s[12:13]
	v_and_b32_e32 v58, v58, v56
	v_cmp_ne_u32_e32 vcc, 0, v58
	s_nop 1
	v_cndmask_b32_e32 v81, v2, v154, vcc
	s_cmp_lg_u64 vcc, 0
	s_cselect_b32 s21, 1, 0
	v_lshrrev_b64 v[58:59], v54, s[14:15]
	v_and_b32_e32 v58, v58, v56
	v_cmp_ne_u32_e32 vcc, 0, v58
	s_nop 1
	v_cndmask_b32_e32 v82, v2, v154, vcc
	s_cmp_lg_u64 vcc, 0
	s_cselect_b32 s32, 1, 0
	s_waitcnt lgkmcnt(0)
	v_sub_f32_e32 v81, v81, v62
	v_sub_f32_e32 v82, v82, v62
	s_waitcnt vmcnt(0)
	s_and_b32 s83, s1, 0x4000
	v_add_u32_e32 v148, s83, v192
	v_add_u32_e32 v149, v148, v195
	v_add_u32_e32 v148, v148, v193
	ds_read_b128 v[116:119], v148
	ds_read_b128 v[120:123], v149
	ds_read_b128 v[124:127], v148 offset:2048
	ds_read_b128 v[128:131], v149 offset:2048
	ds_read_b128 v[132:135], v148 offset:4096
	ds_read_b128 v[136:139], v149 offset:4096
	ds_read_b128 v[140:143], v148 offset:6144
	ds_read_b128 v[144:147], v149 offset:6144
	v_add_u32_e32 v208, s99, v192
	v_add_u32_e32 v209, v208, v195
	v_add_u32_e32 v208, v208, v193
	v_mov_b32_e32 v70, v81
	v_mov_b32_e32 v71, v81
	v_mov_b32_e32 v72, v81
	v_mov_b32_e32 v73, v81
	v_mov_b32_e32 v74, v81
	v_mov_b32_e32 v75, v81
	v_mov_b32_e32 v76, v81
	v_mov_b32_e32 v77, v81
	v_mov_b32_e32 v200, v81
	v_mov_b32_e32 v201, v81
	v_mov_b32_e32 v202, v81
	v_mov_b32_e32 v203, v81
	v_mov_b32_e32 v204, v81
	v_mov_b32_e32 v205, v81
	v_mov_b32_e32 v206, v81
	v_mov_b32_e32 v207, v81
	ds_read_b128 v[38:41], v208
	ds_read_b128 v[42:45], v209
	ds_read_b128 v[46:49], v208 offset:2048
	ds_read_b128 v[50:53], v209 offset:2048
	v_mov_b32_e32 v54, v82
	v_mov_b32_e32 v55, v82
	v_mov_b32_e32 v56, v82
	v_mov_b32_e32 v57, v82
	v_mov_b32_e32 v58, v82
	v_mov_b32_e32 v59, v82
	v_mov_b32_e32 v60, v82
	v_mov_b32_e32 v61, v82
	v_mov_b32_e32 v62, v82
	v_mov_b32_e32 v63, v82
	v_mov_b32_e32 v64, v82
	v_mov_b32_e32 v65, v82
	v_mov_b32_e32 v66, v82
	v_mov_b32_e32 v67, v82
	v_mov_b32_e32 v68, v82
	v_mov_b32_e32 v69, v82
	s_waitcnt lgkmcnt(10)
	v_mfma_f32_16x16x32_bf16 v[70:73], v[116:119], v[104:107], v[70:73]
	v_mfma_f32_16x16x32_bf16 v[70:73], v[120:123], v[108:111], v[70:73]
	s_waitcnt lgkmcnt(8)
	v_mfma_f32_16x16x32_bf16 v[74:77], v[124:127], v[104:107], v[74:77]
	v_mfma_f32_16x16x32_bf16 v[74:77], v[128:131], v[108:111], v[74:77]
	ds_read_b128 v[116:119], v148 offset:32768
	ds_read_b128 v[120:123], v149 offset:32768
	ds_read_b128 v[124:127], v148 offset:34816
	ds_read_b128 v[128:131], v149 offset:34816
	s_waitcnt lgkmcnt(10)
	v_mfma_f32_16x16x32_bf16 v[200:203], v[132:135], v[104:107], v[200:203]
	v_mfma_f32_16x16x32_bf16 v[200:203], v[136:139], v[108:111], v[200:203]
	s_waitcnt lgkmcnt(8)
	v_mfma_f32_16x16x32_bf16 v[204:207], v[140:143], v[104:107], v[204:207]
	v_mfma_f32_16x16x32_bf16 v[204:207], v[144:147], v[108:111], v[204:207]
	ds_read_b128 v[132:135], v148 offset:36864
	ds_read_b128 v[136:139], v149 offset:36864
	ds_read_b128 v[140:143], v148 offset:38912
	ds_read_b128 v[144:147], v149 offset:38912
	s_waitcnt lgkmcnt(10)
	v_mfma_f32_16x16x32_bf16 v[54:57], v[38:41], v[104:107], v[54:57]
	v_mfma_f32_16x16x32_bf16 v[54:57], v[42:45], v[108:111], v[54:57]
	s_waitcnt lgkmcnt(8)
	v_mfma_f32_16x16x32_bf16 v[58:61], v[46:49], v[104:107], v[58:61]
	v_mfma_f32_16x16x32_bf16 v[58:61], v[50:53], v[108:111], v[58:61]
	ds_read_b128 v[38:41], v208 offset:4096
	ds_read_b128 v[42:45], v209 offset:4096
	ds_read_b128 v[46:49], v208 offset:6144
	ds_read_b128 v[50:53], v209 offset:6144
	v_exp_f32_e32 v70, v70
	v_exp_f32_e32 v71, v71
	v_exp_f32_e32 v72, v72
	v_exp_f32_e32 v73, v73
	v_exp_f32_e32 v74, v74
	v_exp_f32_e32 v75, v75
	v_exp_f32_e32 v76, v76
	v_exp_f32_e32 v77, v77
	v_exp_f32_e32 v200, v200
	v_exp_f32_e32 v201, v201
	v_exp_f32_e32 v202, v202
	v_exp_f32_e32 v203, v203
	v_exp_f32_e32 v204, v204
	v_exp_f32_e32 v205, v205
	v_exp_f32_e32 v206, v206
	v_exp_f32_e32 v207, v207
	s_nop 0
	v_cvt_pk_bf16_f32 v70, v70, v71
	v_cvt_pk_bf16_f32 v71, v72, v73
	v_cvt_pk_bf16_f32 v72, v74, v75
	v_cvt_pk_bf16_f32 v73, v76, v77
	v_cvt_pk_bf16_f32 v74, v200, v201
	v_cvt_pk_bf16_f32 v75, v202, v203
	v_cvt_pk_bf16_f32 v76, v204, v205
	v_cvt_pk_bf16_f32 v77, v206, v207
	s_nop 1
	v_mfma_f32_16x16x32_bf16 v[100:103], v[112:115], v[70:73], 0
	v_mfma_f32_16x16x32_bf16 v[100:103], v[112:115], v[74:77], v[100:103]
	s_waitcnt lgkmcnt(4)
; __device__ __forceinline__ float ex2(float x) { return __builtin_amdgcn_exp2f(x); }
; template <bool SELMASK>
; __device__ __forceinline__ void attn_far_fast(const LAS unsigned char* kb, const LAS unsigned char* vb, const bf16x8 (&qf)[2][2], int col, int q, float bias_far, bool sel0, bool sel1, Softmax (&st)[2], f32x4 (&O)[2][4]) {
;     ...
;         for (int kt = 0; kt < 4; ++kt) { f32x4 p = S[c][kt] + off;
; #pragma unroll
;             for (int e = 0; e < 4; ++e) p[e] = ex2(p[e]);
;             S[c][kt] = p; }
;         pf[c][0] = pack8(S[c][0], S[c][1]); pf[c][1] = pack8(S[c][2], S[c][3]);
;         st[c].l = __builtin_amdgcn_mfma_f32_16x16x32_bf16(ONES8, pf[c][0], st[c].l, 0, 0, 0); st[c].l = __builtin_amdgcn_mfma_f32_16x16x32_bf16(ONES8, pf[c][1], st[c].l, 0, 0, 0);
;     }
; #pragma unroll
;     for (int c32 = 0; c32 < 2; ++c32)
; #pragma unroll
;         for (int dt = 0; dt < 4; ++dt) { const bf16x8 vf = lds_frag(vb, 16 * dt + col, 4 * c32 + q);
;             O[0][dt] = __builtin_amdgcn_mfma_f32_16x16x32_bf16(vf, pf[0][c32], O[0][dt], 0, 0, 0);
;             O[1][dt] = __builtin_amdgcn_mfma_f32_16x16x32_bf16(vf, pf[1][c32], O[1][dt], 0, 0, 0); }
	v_mfma_f32_16x16x32_bf16 v[84:87], v[116:119], v[70:73], 0
	v_mfma_f32_16x16x32_bf16 v[84:87], v[120:123], v[74:77], v[84:87]
	v_mfma_f32_16x16x32_bf16 v[88:91], v[124:127], v[70:73], 0
	v_mfma_f32_16x16x32_bf16 v[88:91], v[128:131], v[74:77], v[88:91]
	v_mfma_f32_16x16x32_bf16 v[92:95], v[132:135], v[70:73], 0
	v_mfma_f32_16x16x32_bf16 v[92:95], v[136:139], v[74:77], v[92:95]
	v_mfma_f32_16x16x32_bf16 v[96:99], v[140:143], v[70:73], 0
	v_mfma_f32_16x16x32_bf16 v[96:99], v[144:147], v[74:77], v[96:99]
	s_waitcnt lgkmcnt(2)
	v_mfma_f32_16x16x32_bf16 v[62:65], v[38:41], v[104:107], v[62:65]
	v_mfma_f32_16x16x32_bf16 v[62:65], v[42:45], v[108:111], v[62:65]
	s_waitcnt lgkmcnt(0)
	v_mfma_f32_16x16x32_bf16 v[66:69], v[46:49], v[104:107], v[66:69]
	v_mfma_f32_16x16x32_bf16 v[66:69], v[50:53], v[108:111], v[66:69]
	ds_read_b128 v[116:119], v208 offset:32768
	ds_read_b128 v[120:123], v209 offset:32768
	ds_read_b128 v[124:127], v208 offset:34816
	ds_read_b128 v[128:131], v209 offset:34816
	ds_read_b128 v[132:135], v208 offset:36864
	ds_read_b128 v[136:139], v209 offset:36864
	ds_read_b128 v[140:143], v208 offset:38912
	ds_read_b128 v[144:147], v209 offset:38912
	s_nop 3
	v_exp_f32_e32 v54, v54
	v_exp_f32_e32 v55, v55
	v_exp_f32_e32 v56, v56
	v_exp_f32_e32 v57, v57
	v_exp_f32_e32 v58, v58
	v_exp_f32_e32 v59, v59
	v_exp_f32_e32 v60, v60
	v_exp_f32_e32 v61, v61
	v_exp_f32_e32 v62, v62
	v_exp_f32_e32 v63, v63
	v_exp_f32_e32 v64, v64
	v_exp_f32_e32 v65, v65
	v_exp_f32_e32 v66, v66
	v_exp_f32_e32 v67, v67
	v_exp_f32_e32 v68, v68
	v_exp_f32_e32 v69, v69
	s_nop 0
	v_cvt_pk_bf16_f32 v54, v54, v55
	v_cvt_pk_bf16_f32 v55, v56, v57
	v_cvt_pk_bf16_f32 v56, v58, v59
	v_cvt_pk_bf16_f32 v57, v60, v61
	v_cvt_pk_bf16_f32 v58, v62, v63
	v_cvt_pk_bf16_f32 v59, v64, v65
	v_cvt_pk_bf16_f32 v60, v66, v67
	v_cvt_pk_bf16_f32 v61, v68, v69
	s_nop 1
	v_mfma_f32_16x16x32_bf16 v[100:103], v[112:115], v[54:57], v[100:103]
	v_mfma_f32_16x16x32_bf16 v[100:103], v[112:115], v[58:61], v[100:103]
	s_waitcnt lgkmcnt(4)
	v_mfma_f32_16x16x32_bf16 v[84:87], v[116:119], v[54:57], v[84:87]
	v_mfma_f32_16x16x32_bf16 v[84:87], v[120:123], v[58:61], v[84:87]
	v_mfma_f32_16x16x32_bf16 v[88:91], v[124:127], v[54:57], v[88:91]
	v_mfma_f32_16x16x32_bf16 v[88:91], v[128:131], v[58:61], v[88:91]
	v_lshlrev_b32_e32 v254, 6, v186
	v_sub_u32_e32 v254, v83, v254
	ds_read2_b32 v[200:201], v83 offset0:0 offset1:4
	ds_read2_b32 v[202:203], v83 offset0:8 offset1:12
	ds_read2_b32 v[204:205], v83 offset0:64 offset1:68
	ds_read2_b32 v[206:207], v83 offset0:72 offset1:76
	ds_read2_b32 v[62:63], v83 offset0:128 offset1:132
	ds_read2_b32 v[64:65], v83 offset0:136 offset1:140
	ds_read2_b32 v[66:67], v83 offset0:192 offset1:196
	ds_read2_b32 v[68:69], v83 offset0:200 offset1:204
	ds_read_b32 v199, v254 offset:1024
	s_waitcnt lgkmcnt(9)
	v_mfma_f32_16x16x32_bf16 v[92:95], v[132:135], v[54:57], v[92:95]
	v_mfma_f32_16x16x32_bf16 v[92:95], v[136:139], v[58:61], v[92:95]
	v_mfma_f32_16x16x32_bf16 v[96:99], v[140:143], v[54:57], v[96:99]
	v_mfma_f32_16x16x32_bf16 v[96:99], v[144:147], v[58:61], v[96:99]
	s_nop 1
	s_waitcnt lgkmcnt(0)
	v_add_f32_e32 v200, v200, v84
	v_add_f32_e32 v201, v201, v85
	v_add_f32_e32 v202, v202, v86
	v_add_f32_e32 v203, v203, v87
	v_add_f32_e32 v204, v204, v88
	v_add_f32_e32 v205, v205, v89
	v_add_f32_e32 v206, v206, v90
	v_add_f32_e32 v207, v207, v91
	v_add_f32_e32 v199, v199, v100
	v_add_f32_e32 v62, v62, v92
	v_add_f32_e32 v63, v63, v93
	v_add_f32_e32 v64, v64, v94
	v_add_f32_e32 v65, v65, v95
	v_add_f32_e32 v66, v66, v96
	v_add_f32_e32 v67, v67, v97
	v_add_f32_e32 v68, v68, v98
	v_add_f32_e32 v69, v69, v99
	v_cmp_ne_u32_e32 vcc, 0, v79
	s_and_saveexec_b64 s[84:85], vcc
	ds_write2_b32 v83, v200, v201 offset0:0 offset1:4
	ds_write2_b32 v83, v202, v203 offset0:8 offset1:12
	ds_write2_b32 v83, v204, v205 offset0:64 offset1:68
	ds_write2_b32 v83, v206, v207 offset0:72 offset1:76
	ds_write2_b32 v83, v62, v63 offset0:128 offset1:132
	ds_write2_b32 v83, v64, v65 offset0:136 offset1:140
	ds_write2_b32 v83, v66, v67 offset0:192 offset1:196
	ds_write2_b32 v83, v68, v69 offset0:200 offset1:204
	ds_write_b32 v254, v199 offset:1024
	s_mov_b64 exec, s[84:85]
	s_nop 3

.Lbm_noitem:
	s_mov_b32 s100, -1
	s_add_i32 s83, s75, 2
	s_cmp_gt_i32 s83, s26
	s_cbranch_scc1 .Lbm_pf_end_b
	s_lshr_b32 s21, s83, 5
	v_mov_b32_e32 v81, v242
	s_cmp_eq_u32 s21, 1
	s_cselect_b64 vcc, -1, 0
	v_cndmask_b32_e32 v81, v81, v243, vcc
	s_cmp_eq_u32 s21, 2
	s_cselect_b64 vcc, -1, 0
	v_cndmask_b32_e32 v81, v81, v244, vcc
	s_cmp_eq_u32 s21, 3
	s_cselect_b64 vcc, -1, 0
	v_cndmask_b32_e32 v81, v81, v245, vcc
	s_and_b32 s21, s83, 31
	s_lshl_b32 s21, 1, s21
	s_lshl_b32 s32, s21, 1
	v_and_b32_e32 v80, s21, v81
	v_cmp_ne_u32_e64 s[12:13], 0, v80
	v_and_b32_e32 v80, s32, v81
	v_cmp_ne_u32_e64 s[14:15], 0, v80
	s_nop 3
	s_or_b64 s[22:23], s[12:13], s[14:15]
	s_bcnt1_i32_b64 s11, s[22:23]
	s_add_i32 s11, s11, 3
	s_lshr_b32 s11, s11, 2
	s_mov_b32 s21, s91
	s_cmp_ge_u32 s21, s11
	s_cbranch_scc1 .Lbm_pf_end_b
	s_andn2_b64 s[84:85], s[12:13], s[14:15]
	s_bcnt1_i32_b64 s77, s[84:85]
	v_mbcnt_lo_u32_b32 v80, s84, 0
	v_mbcnt_hi_u32_b32 v80, s85, v80
	v_mov_b32_e32 v81, s77
	s_and_b64 s[84:85], s[12:13], s[14:15]
	s_bcnt1_i32_b64 s32, s[84:85]
	v_mbcnt_lo_u32_b32 v81, s84, v81
	v_mbcnt_hi_u32_b32 v81, s85, v81
	s_add_i32 s77, s77, s32
	v_cndmask_b32_e64 v80, v80, v81, s[84:85]
	v_mov_b32_e32 v81, s77
	s_andn2_b64 s[84:85], s[14:15], s[12:13]
	v_mbcnt_lo_u32_b32 v81, s84, v81
	v_mbcnt_hi_u32_b32 v81, s85, v81
	s_nop 0
	v_cndmask_b32_e64 v80, v80, v81, s[84:85]
	s_lshl_b32 s32, s21, 2
	v_mov_b32_e32 v199, -1
	s_add_i32 s77, s32, 0
	v_cmp_eq_u32_e64 s[84:85], s77, v80
	s_nop 3
	s_and_b64 s[84:85], s[84:85], s[22:23]
	s_ff1_i32_b64 s77, s[84:85]
	v_writelane_b32 v199, s77, 0
	s_add_i32 s77, s32, 1
	v_cmp_eq_u32_e64 s[84:85], s77, v80
	s_nop 3
	s_and_b64 s[84:85], s[84:85], s[22:23]
	s_ff1_i32_b64 s77, s[84:85]
	v_writelane_b32 v199, s77, 1
	s_add_i32 s77, s32, 2
	v_cmp_eq_u32_e64 s[84:85], s77, v80
	s_nop 3
	s_and_b64 s[84:85], s[84:85], s[22:23]
	s_ff1_i32_b64 s77, s[84:85]
	v_writelane_b32 v199, s77, 2
	s_add_i32 s77, s32, 3
	v_cmp_eq_u32_e64 s[84:85], s77, v80
	s_nop 3
	s_and_b64 s[84:85], s[84:85], s[22:23]
	s_ff1_i32_b64 s77, s[84:85]
	v_writelane_b32 v199, s77, 3
	ds_bpermute_b32 v251, v250, v199
	s_waitcnt lgkmcnt(0)
	v_max_i32_e32 v208, 0, v251
	v_lshlrev_b32_e32 v208, 11, v208
	v_mov_b32_e32 v209, 0
	v_lshl_add_u64 v[254:255], v[208:209], 0, v[246:247]
	global_load_dwordx4 v[104:107], v[254:255], off
	global_load_dwordx4 v[108:111], v[254:255], off offset:64
	s_mov_b32 s100, s83

.Lbm_join1:
	ds_write_b128 v78, v[26:29]
	ds_write_b128 v78, v[22:25] offset:32768
	s_add_i32 s10, s1, 0x6000
	s_and_b32 s10, s10, 0x6000
	v_add_u32_e32 v78, s10, v188
	ds_write_b128 v78, v[30:33]
	ds_write_b128 v78, v[34:37] offset:32768
	s_mov_b32 s101, 0
	s_cmp_ge_i32 s75, s26
	s_cbranch_scc1 .LBB0_1228
	s_add_u32 s12, s64, 0x10000
	s_addc_u32 s13, s65, 0
	s_add_u32 s14, s62, 0x100
	s_addc_u32 s15, s63, 0
	v_lshl_add_u64 v[78:79], s[14:15], 0, v[162:163]
	v_lshl_add_u64 v[80:81], s[12:13], 0, v[156:157]
	v_lshl_add_u64 v[82:83], s[12:13], 0, v[166:167]
	v_lshl_add_u64 v[254:255], s[14:15], 0, v[168:169]
	v_lshl_add_u64 v[78:79], v[78:79], 0, v[160:161]
	v_lshl_add_u64 v[80:81], v[80:81], 0, v[160:161]
	v_add_co_u32_e32 v82, vcc, 0x8000, v82
	s_nop 1
	v_addc_co_u32_e32 v83, vcc, 0, v83, vcc
	global_load_dwordx4 v[22:25], v[78:79], off
	global_load_dwordx4 v[26:29], v[80:81], off
	global_load_dwordx4 v[30:33], v[82:83], off
	global_load_dwordx4 v[34:37], v[254:255], off offset:128
	s_mov_b32 s101, 1
	s_branch .LBB0_1228
